# phase 12 tail: final_g tiles loaded together, 8 output stores back to back (no per-store vmcnt(0)); on top of v25
# baseline (speedup 1.0000x reference)
; #define GAS __attribute__((address_space(1)))
; __device__ __forceinline__ f32x4 unpack4(u32x2 w) { return (f32x4){bflo(w.x), bfhi(w.x), bflo(w.y), bfhi(w.y)}; }
; __device__ __forceinline__ void phase12(KP kp, LAS unsigned char* lds, int wave, int bid, int G) {
;     ...
;     for (int m = bid * NWAVES + wave; m < T; m += G * NWAVES) {
;         const GAS f32x4* xr = (const GAS f32x4*)(X1 + (size_t)m * DM) + lane;
;         const i32x4 te = *(const GAS i32x4*)(TOPI + m * 4), rk = *(const GAS i32x4*)(TRANK + m * 4); const f32x4 tw = *(const GAS f32x4*)(TOPW + m * 4);
;         const i32x4 sl = (i32x4){pstart[te.x] + rk.x, pstart[te.y] + rk.y, pstart[te.z] + rk.z, pstart[te.w] + rk.w};
;         const GAS u32x2* y0 = (const GAS u32x2*)(YS + (size_t)sl.x * DM) + lane; const GAS u32x2* y1 = (const GAS u32x2*)(YS + (size_t)sl.y * DM) + lane;
;         const GAS u32x2* y2 = (const GAS u32x2*)(YS + (size_t)sl.z * DM) + lane; const GAS u32x2* y3 = (const GAS u32x2*)(YS + (size_t)sl.w * DM) + lane;
;         f32x4 v[8]; float s = 0.f;
; #pragma unroll
;         for (int j = 0; j < 8; ++j) {
;             const f32x4 mo = tw.x * unpack4(y0[64 * j]) + tw.y * unpack4(y1[64 * j]) + tw.z * unpack4(y2[64 * j]) + tw.w * unpack4(y3[64 * j]);
.LBB0_4682:
	v_lshl_add_u64 v[36:37], s[12:13], 0, v[90:91]
	s_ashr_i32 s5, s4, 31
	v_add_co_u32_e32 v104, vcc, s7, v36
	s_lshl_b64 s[0:1], s[4:5], 2
	s_nop 0
	v_addc_co_u32_e32 v105, vcc, 0, v37, vcc
	v_add_co_u32_e32 v106, vcc, s21, v36
	s_add_u32 s24, s14, s0
	s_nop 0
	v_addc_co_u32_e32 v107, vcc, 0, v37, vcc
	s_addc_u32 s25, s15, s1
	global_load_dwordx4 v[0:3], v[70:71], off
	global_load_dwordx4 v[4:7], v[70:71], off offset:1024
	global_load_dwordx4 v[8:11], v[70:71], off offset:2048
	global_load_dwordx4 v[12:15], v[70:71], off offset:3072
	global_load_dwordx4 v[16:19], v[74:75], off
	global_load_dwordx4 v[20:23], v[76:77], off
	global_load_dwordx4 v[24:27], v[78:79], off
	global_load_dwordx4 v[32:35], v[80:81], off
	global_load_dwordx4 v[28:31], v[72:73], off
	global_load_dwordx4 v[60:63], v[104:105], off offset:1024
	global_load_dwordx4 v[56:59], v[104:105], off offset:2048
	global_load_dwordx4 v[48:51], v[104:105], off offset:3072
	global_load_dwordx4 v[64:67], v[106:107], off offset:-4096
	global_load_dwordx4 v[52:55], v[106:107], off
	global_load_dwordx4 v[44:47], v[106:107], off offset:1024
	global_load_dwordx4 v[40:43], v[106:107], off offset:2048
	global_load_dwordx4 v[36:39], v[106:107], off offset:3072
	v_lshl_add_u64 v[92:93], s[8:9], 0, v[90:91]
	global_load_dwordx4 v[104:107], v100, s[24:25]
	s_add_u32 s24, s17, s0
	s_addc_u32 s25, s18, s1
	global_load_dwordx4 v[108:111], v100, s[24:25]
	s_add_u32 s0, s19, s0
	s_addc_u32 s1, s20, s1
	global_load_dwordx4 v[112:115], v100, s[0:1]
	s_add_i32 s2, s2, s6
	s_add_i32 s4, s4, s16
	s_add_u32 s8, s8, s10
	s_addc_u32 s9, s9, s11
	s_add_u32 s12, s12, s10
	s_addc_u32 s13, s13, s11
	s_cmpk_lt_i32 s2, 0x2000
	s_waitcnt vmcnt(2)
	v_lshlrev_b32_e32 v103, 2, v104
	v_lshlrev_b32_e32 v104, 2, v105
	v_lshlrev_b32_e32 v105, 2, v106
	v_lshlrev_b32_e32 v106, 2, v107
	v_add_u32_e32 v103, s3, v103
	v_add_u32_e32 v105, s3, v105
	v_add_u32_e32 v104, s3, v104
	v_add_u32_e32 v106, s3, v106
	ds_read_b32 v103, v103
	ds_read_b32 v107, v104
	ds_read_b32 v105, v105
	ds_read_b32 v116, v106
	s_waitcnt vmcnt(0)
	v_mov_b32_e32 v104, v115
	s_waitcnt lgkmcnt(3)
	v_add_u32_e32 v106, v103, v108
	s_waitcnt lgkmcnt(2)
	v_add_u32_e32 v108, v107, v109
	s_waitcnt lgkmcnt(1)
	v_add_u32_e32 v110, v105, v110
	s_waitcnt lgkmcnt(0)
	v_add_u32_e32 v116, v116, v111
	v_ashrrev_i32_e32 v107, 31, v106
	v_ashrrev_i32_e32 v109, 31, v108
	v_ashrrev_i32_e32 v111, 31, v110
	v_ashrrev_i32_e32 v117, 31, v116
	v_lshlrev_b64 v[106:107], 12, v[106:107]
	v_lshlrev_b64 v[108:109], 12, v[108:109]
	v_lshlrev_b64 v[110:111], 12, v[110:111]
	v_lshlrev_b64 v[116:117], 12, v[116:117]
	v_lshl_add_u64 v[106:107], v[68:69], 0, v[106:107]
	v_lshl_add_u64 v[108:109], v[68:69], 0, v[108:109]
	v_lshl_add_u64 v[110:111], v[68:69], 0, v[110:111]
	v_lshl_add_u64 v[116:117], v[68:69], 0, v[116:117]
	global_load_dwordx2 v[118:119], v[106:107], off
	global_load_dwordx2 v[120:121], v[108:109], off
	global_load_dwordx2 v[122:123], v[110:111], off
	global_load_dwordx2 v[124:125], v[116:117], off
	global_load_dwordx2 v[126:127], v[106:107], off offset:512
	global_load_dwordx2 v[128:129], v[108:109], off offset:512
	global_load_dwordx2 v[130:131], v[110:111], off offset:512
	global_load_dwordx2 v[132:133], v[116:117], off offset:512
	global_load_dwordx2 v[134:135], v[106:107], off offset:1024
	global_load_dwordx2 v[136:137], v[108:109], off offset:1024
	global_load_dwordx2 v[138:139], v[110:111], off offset:1024
	global_load_dwordx2 v[140:141], v[116:117], off offset:1024
	global_load_dwordx2 v[142:143], v[106:107], off offset:1536
	global_load_dwordx2 v[144:145], v[108:109], off offset:1536
	global_load_dwordx2 v[146:147], v[110:111], off offset:1536
	global_load_dwordx2 v[148:149], v[116:117], off offset:1536
	global_load_dwordx2 v[150:151], v[106:107], off offset:2048
	global_load_dwordx2 v[152:153], v[106:107], off offset:2560
	global_load_dwordx2 v[154:155], v[106:107], off offset:3072
	s_nop 0
	global_load_dwordx2 v[106:107], v[106:107], off offset:3584
	s_nop 0
	global_load_dwordx2 v[156:157], v[108:109], off offset:2048
	global_load_dwordx2 v[158:159], v[108:109], off offset:2560
	global_load_dwordx2 v[160:161], v[108:109], off offset:3072
	s_nop 0
	global_load_dwordx2 v[108:109], v[108:109], off offset:3584
	s_nop 0
	global_load_dwordx2 v[162:163], v[110:111], off offset:2048
	global_load_dwordx2 v[164:165], v[110:111], off offset:2560
	global_load_dwordx2 v[166:167], v[110:111], off offset:3072
	s_nop 0
	global_load_dwordx2 v[110:111], v[110:111], off offset:3584
	s_nop 0
	global_load_dwordx2 v[168:169], v[116:117], off offset:2048
	global_load_dwordx2 v[170:171], v[116:117], off offset:2560
	global_load_dwordx2 v[172:173], v[116:117], off offset:3072
	s_nop 0
	global_load_dwordx2 v[116:117], v[116:117], off offset:3584
	s_waitcnt vmcnt(31)
	v_lshlrev_b32_e32 v174, 16, v118
	s_waitcnt vmcnt(30)
	v_lshlrev_b32_e32 v176, 16, v120
	v_and_b32_e32 v177, 0xffff0000, v120
	v_lshlrev_b32_e32 v120, 16, v121
	v_and_b32_e32 v121, 0xffff0000, v121
	s_waitcnt vmcnt(26)
	v_lshlrev_b32_e32 v184, 16, v128
	v_and_b32_e32 v185, 0xffff0000, v128
	v_lshlrev_b32_e32 v128, 16, v129
	v_and_b32_e32 v129, 0xffff0000, v129
	v_and_b32_e32 v175, 0xffff0000, v118
	v_lshlrev_b32_e32 v118, 16, v119
	v_and_b32_e32 v119, 0xffff0000, v119
	v_lshlrev_b32_e32 v182, 16, v126
	v_and_b32_e32 v183, 0xffff0000, v126
	v_lshlrev_b32_e32 v126, 16, v127
	v_and_b32_e32 v127, 0xffff0000, v127
	s_waitcnt vmcnt(22)
	v_lshlrev_b32_e32 v192, 16, v136
	v_and_b32_e32 v193, 0xffff0000, v136
	v_lshlrev_b32_e32 v136, 16, v137
	v_and_b32_e32 v137, 0xffff0000, v137
	s_waitcnt vmcnt(18)
; __device__ __forceinline__ float bflo(unsigned w) { return __uint_as_float(w << 16); }
; __device__ __forceinline__ float bfhi(unsigned w) { return __uint_as_float(w & 0xffff0000u); }
; __device__ __forceinline__ f32x4 unpack4(u32x2 w) { return (f32x4){bflo(w.x), bfhi(w.x), bflo(w.y), bfhi(w.y)}; }
; __device__ __forceinline__ void phase12(KP kp, LAS unsigned char* lds, int wave, int bid, int G) {
;     ...
;         for (int j = 0; j < 8; ++j) {
;             const f32x4 mo = tw.x * unpack4(y0[64 * j]) + tw.y * unpack4(y1[64 * j]) + tw.z * unpack4(y2[64 * j]) + tw.w * unpack4(y3[64 * j]);
	v_lshlrev_b32_e32 v200, 16, v144
	v_and_b32_e32 v201, 0xffff0000, v144
	v_lshlrev_b32_e32 v144, 16, v145
	v_and_b32_e32 v145, 0xffff0000, v145
	s_waitcnt vmcnt(11)
	v_lshlrev_b32_e32 v208, 16, v156
	v_and_b32_e32 v209, 0xffff0000, v156
	v_lshlrev_b32_e32 v156, 16, v157
	v_and_b32_e32 v157, 0xffff0000, v157
	s_waitcnt vmcnt(10)
	v_lshlrev_b32_e32 v216, 16, v158
	v_and_b32_e32 v217, 0xffff0000, v158
	v_lshlrev_b32_e32 v158, 16, v159
	v_and_b32_e32 v159, 0xffff0000, v159
	s_waitcnt vmcnt(9)
	v_lshlrev_b32_e32 v224, 16, v160
	v_and_b32_e32 v225, 0xffff0000, v160
	v_lshlrev_b32_e32 v160, 16, v161
	v_and_b32_e32 v161, 0xffff0000, v161
	s_waitcnt vmcnt(8)
	v_lshlrev_b32_e32 v232, 16, v108
	v_and_b32_e32 v233, 0xffff0000, v108
	v_lshlrev_b32_e32 v108, 16, v109
	v_and_b32_e32 v109, 0xffff0000, v109
	v_pk_mul_f32 v[120:121], v[112:113], v[120:121] op_sel:[1,0]
	v_pk_mul_f32 v[176:177], v[112:113], v[176:177] op_sel:[1,0]
	v_pk_mul_f32 v[128:129], v[112:113], v[128:129] op_sel:[1,0]
	v_pk_mul_f32 v[184:185], v[112:113], v[184:185] op_sel:[1,0]
	v_lshlrev_b32_e32 v178, 16, v122
	v_and_b32_e32 v179, 0xffff0000, v122
	v_lshlrev_b32_e32 v122, 16, v123
	v_and_b32_e32 v123, 0xffff0000, v123
	v_lshlrev_b32_e32 v186, 16, v130
	v_and_b32_e32 v187, 0xffff0000, v130
	v_lshlrev_b32_e32 v130, 16, v131
	v_and_b32_e32 v131, 0xffff0000, v131
	v_lshlrev_b32_e32 v190, 16, v134
	v_and_b32_e32 v191, 0xffff0000, v134
	v_lshlrev_b32_e32 v134, 16, v135
	v_and_b32_e32 v135, 0xffff0000, v135
	v_lshlrev_b32_e32 v198, 16, v142
	v_and_b32_e32 v199, 0xffff0000, v142
	v_lshlrev_b32_e32 v142, 16, v143
	v_and_b32_e32 v143, 0xffff0000, v143
	v_lshlrev_b32_e32 v206, 16, v150
	v_and_b32_e32 v207, 0xffff0000, v150
	v_lshlrev_b32_e32 v150, 16, v151
	v_and_b32_e32 v151, 0xffff0000, v151
	v_lshlrev_b32_e32 v214, 16, v152
	v_and_b32_e32 v215, 0xffff0000, v152
	v_lshlrev_b32_e32 v152, 16, v153
	v_and_b32_e32 v153, 0xffff0000, v153
	v_lshlrev_b32_e32 v222, 16, v154
	v_and_b32_e32 v223, 0xffff0000, v154
	v_lshlrev_b32_e32 v154, 16, v155
	v_and_b32_e32 v155, 0xffff0000, v155
	v_lshlrev_b32_e32 v230, 16, v106
	v_and_b32_e32 v231, 0xffff0000, v106
	v_lshlrev_b32_e32 v106, 16, v107
	v_and_b32_e32 v107, 0xffff0000, v107
	v_pk_mul_f32 v[192:193], v[112:113], v[192:193] op_sel:[1,0]
	v_pk_mul_f32 v[136:137], v[112:113], v[136:137] op_sel:[1,0]
	v_pk_mul_f32 v[144:145], v[112:113], v[144:145] op_sel:[1,0]
	v_pk_mul_f32 v[200:201], v[112:113], v[200:201] op_sel:[1,0]
	v_pk_mul_f32 v[156:157], v[112:113], v[156:157] op_sel:[1,0]
	v_pk_mul_f32 v[208:209], v[112:113], v[208:209] op_sel:[1,0]
	v_pk_mul_f32 v[216:217], v[112:113], v[216:217] op_sel:[1,0]
	v_pk_mul_f32 v[158:159], v[112:113], v[158:159] op_sel:[1,0]
	v_pk_mul_f32 v[160:161], v[112:113], v[160:161] op_sel:[1,0]
	v_pk_mul_f32 v[224:225], v[112:113], v[224:225] op_sel:[1,0]
	v_pk_mul_f32 v[108:109], v[112:113], v[108:109] op_sel:[1,0]
	v_pk_mul_f32 v[232:233], v[112:113], v[232:233] op_sel:[1,0]
	v_pk_fma_f32 v[174:175], v[112:113], v[174:175], v[176:177] op_sel_hi:[0,1,1]
	v_pk_fma_f32 v[118:119], v[112:113], v[118:119], v[120:121] op_sel_hi:[0,1,1]
	v_pk_fma_f32 v[120:121], v[112:113], v[182:183], v[184:185] op_sel_hi:[0,1,1]
	v_pk_fma_f32 v[126:127], v[112:113], v[126:127], v[128:129] op_sel_hi:[0,1,1]
	v_lshlrev_b32_e32 v180, 16, v124
	v_and_b32_e32 v181, 0xffff0000, v124
	v_lshlrev_b32_e32 v124, 16, v125
	v_and_b32_e32 v125, 0xffff0000, v125
	v_lshlrev_b32_e32 v188, 16, v132
	v_and_b32_e32 v189, 0xffff0000, v132
	v_lshlrev_b32_e32 v132, 16, v133
	v_and_b32_e32 v133, 0xffff0000, v133
	v_lshlrev_b32_e32 v194, 16, v138
	v_and_b32_e32 v195, 0xffff0000, v138
	v_lshlrev_b32_e32 v138, 16, v139
	v_and_b32_e32 v139, 0xffff0000, v139
	v_lshlrev_b32_e32 v202, 16, v146
	v_and_b32_e32 v203, 0xffff0000, v146
	v_lshlrev_b32_e32 v146, 16, v147
	v_and_b32_e32 v147, 0xffff0000, v147
	s_waitcnt vmcnt(7)
	v_lshlrev_b32_e32 v210, 16, v162
	v_and_b32_e32 v211, 0xffff0000, v162
	v_lshlrev_b32_e32 v162, 16, v163
	v_and_b32_e32 v163, 0xffff0000, v163
	s_waitcnt vmcnt(6)
	v_lshlrev_b32_e32 v218, 16, v164
	v_and_b32_e32 v219, 0xffff0000, v164
	v_lshlrev_b32_e32 v164, 16, v165
	v_and_b32_e32 v165, 0xffff0000, v165
	s_waitcnt vmcnt(5)
	v_lshlrev_b32_e32 v226, 16, v166
	v_and_b32_e32 v227, 0xffff0000, v166
	v_lshlrev_b32_e32 v166, 16, v167
	v_and_b32_e32 v167, 0xffff0000, v167
	s_waitcnt vmcnt(4)
	v_lshlrev_b32_e32 v234, 16, v110
	v_and_b32_e32 v235, 0xffff0000, v110
	v_lshlrev_b32_e32 v110, 16, v111
	v_and_b32_e32 v111, 0xffff0000, v111
	v_pk_fma_f32 v[128:129], v[112:113], v[134:135], v[136:137] op_sel_hi:[0,1,1]
	v_pk_fma_f32 v[134:135], v[112:113], v[190:191], v[192:193] op_sel_hi:[0,1,1]
	v_pk_fma_f32 v[136:137], v[112:113], v[198:199], v[200:201] op_sel_hi:[0,1,1]
	v_pk_fma_f32 v[142:143], v[112:113], v[142:143], v[144:145] op_sel_hi:[0,1,1]
	v_pk_fma_f32 v[144:145], v[112:113], v[206:207], v[208:209] op_sel_hi:[0,1,1]
	v_pk_fma_f32 v[150:151], v[112:113], v[150:151], v[156:157] op_sel_hi:[0,1,1]
	v_pk_fma_f32 v[152:153], v[112:113], v[152:153], v[158:159] op_sel_hi:[0,1,1]
	v_pk_fma_f32 v[156:157], v[112:113], v[214:215], v[216:217] op_sel_hi:[0,1,1]
	v_pk_fma_f32 v[158:159], v[112:113], v[222:223], v[224:225] op_sel_hi:[0,1,1]
	v_pk_fma_f32 v[154:155], v[112:113], v[154:155], v[160:161] op_sel_hi:[0,1,1]
	v_pk_fma_f32 v[160:161], v[112:113], v[230:231], v[232:233] op_sel_hi:[0,1,1]
	v_pk_fma_f32 v[106:107], v[112:113], v[106:107], v[108:109] op_sel_hi:[0,1,1]
	v_pk_fma_f32 v[108:109], v[114:115], v[122:123], v[118:119] op_sel_hi:[0,1,1]
	v_pk_fma_f32 v[112:113], v[114:115], v[178:179], v[174:175] op_sel_hi:[0,1,1]
	v_pk_fma_f32 v[118:119], v[114:115], v[130:131], v[126:127] op_sel_hi:[0,1,1]
	v_pk_fma_f32 v[120:121], v[114:115], v[186:187], v[120:121] op_sel_hi:[0,1,1]
	v_lshlrev_b32_e32 v196, 16, v140
	v_and_b32_e32 v197, 0xffff0000, v140
	v_lshlrev_b32_e32 v140, 16, v141
	v_and_b32_e32 v141, 0xffff0000, v141
	v_lshlrev_b32_e32 v204, 16, v148
	v_and_b32_e32 v205, 0xffff0000, v148
	v_lshlrev_b32_e32 v148, 16, v149
	v_and_b32_e32 v149, 0xffff0000, v149
	s_waitcnt vmcnt(3)
; #define GAS __attribute__((address_space(1)))
; __device__ __forceinline__ float dot4(f32x4 a, f32x4 b) { return (a.x * b.x + a.y * b.y) + (a.z * b.z + a.w * b.w); }
; __device__ __forceinline__ f32x4 unpack4(u32x2 w) { return (f32x4){bflo(w.x), bfhi(w.x), bflo(w.y), bfhi(w.y)}; }
; __device__ __forceinline__ void phase12(KP kp, LAS unsigned char* lds, int wave, int bid, int G) {
;     ...
;             const f32x4 mo = tw.x * unpack4(y0[64 * j]) + tw.y * unpack4(y1[64 * j]) + tw.z * unpack4(y2[64 * j]) + tw.w * unpack4(y3[64 * j]);
;             const f32x4 g2 = *(const GAS f32x4*)(mod + 5 * 2048 + 256 * j + 4 * lane);
;             v[j] = xr[64 * j] + g2 * mo; s += dot4(v[j], v[j]); }
	v_lshlrev_b32_e32 v212, 16, v168
	v_and_b32_e32 v213, 0xffff0000, v168
	v_lshlrev_b32_e32 v168, 16, v169
	v_and_b32_e32 v169, 0xffff0000, v169
	s_waitcnt vmcnt(2)
	v_lshlrev_b32_e32 v220, 16, v170
	v_and_b32_e32 v221, 0xffff0000, v170
	v_lshlrev_b32_e32 v170, 16, v171
	v_and_b32_e32 v171, 0xffff0000, v171
	s_waitcnt vmcnt(1)
	v_lshlrev_b32_e32 v228, 16, v172
	v_and_b32_e32 v229, 0xffff0000, v172
	v_lshlrev_b32_e32 v172, 16, v173
	v_and_b32_e32 v173, 0xffff0000, v173
	s_waitcnt vmcnt(0)
	v_lshlrev_b32_e32 v236, 16, v116
	v_and_b32_e32 v237, 0xffff0000, v116
	v_lshlrev_b32_e32 v116, 16, v117
	v_and_b32_e32 v117, 0xffff0000, v117
	v_pk_fma_f32 v[122:123], v[114:115], v[194:195], v[134:135] op_sel_hi:[0,1,1]
	v_pk_fma_f32 v[126:127], v[114:115], v[138:139], v[128:129] op_sel_hi:[0,1,1]
	v_pk_fma_f32 v[128:129], v[114:115], v[146:147], v[142:143] op_sel_hi:[0,1,1]
	v_pk_fma_f32 v[130:131], v[114:115], v[202:203], v[136:137] op_sel_hi:[0,1,1]
	v_pk_fma_f32 v[134:135], v[114:115], v[162:163], v[150:151] op_sel_hi:[0,1,1]
	v_pk_fma_f32 v[136:137], v[114:115], v[210:211], v[144:145] op_sel_hi:[0,1,1]
	v_pk_fma_f32 v[138:139], v[114:115], v[218:219], v[156:157] op_sel_hi:[0,1,1]
	v_pk_fma_f32 v[142:143], v[114:115], v[164:165], v[152:153] op_sel_hi:[0,1,1]
	v_pk_fma_f32 v[144:145], v[114:115], v[166:167], v[154:155] op_sel_hi:[0,1,1]
	v_pk_fma_f32 v[146:147], v[114:115], v[226:227], v[158:159] op_sel_hi:[0,1,1]
	v_pk_fma_f32 v[106:107], v[114:115], v[110:111], v[106:107] op_sel_hi:[0,1,1]
	v_pk_fma_f32 v[110:111], v[114:115], v[234:235], v[160:161] op_sel_hi:[0,1,1]
	v_pk_fma_f32 v[112:113], v[104:105], v[180:181], v[112:113] op_sel_hi:[0,1,1]
	v_pk_fma_f32 v[108:109], v[104:105], v[124:125], v[108:109] op_sel_hi:[0,1,1]
	v_pk_fma_f32 v[114:115], v[104:105], v[188:189], v[120:121] op_sel_hi:[0,1,1]
	v_pk_fma_f32 v[118:119], v[104:105], v[132:133], v[118:119] op_sel_hi:[0,1,1]
	v_pk_fma_f32 v[120:121], v[104:105], v[140:141], v[126:127] op_sel_hi:[0,1,1]
	v_pk_fma_f32 v[122:123], v[104:105], v[196:197], v[122:123] op_sel_hi:[0,1,1]
	v_pk_fma_f32 v[124:125], v[104:105], v[204:205], v[130:131] op_sel_hi:[0,1,1]
	v_pk_fma_f32 v[126:127], v[104:105], v[148:149], v[128:129] op_sel_hi:[0,1,1]
	v_pk_fma_f32 v[128:129], v[104:105], v[212:213], v[136:137] op_sel_hi:[0,1,1]
	v_pk_fma_f32 v[130:131], v[104:105], v[168:169], v[134:135] op_sel_hi:[0,1,1]
	v_pk_fma_f32 v[132:133], v[104:105], v[170:171], v[142:143] op_sel_hi:[0,1,1]
	v_pk_fma_f32 v[134:135], v[104:105], v[220:221], v[138:139] op_sel_hi:[0,1,1]
	v_pk_fma_f32 v[136:137], v[104:105], v[228:229], v[146:147] op_sel_hi:[0,1,1]
	v_pk_fma_f32 v[138:139], v[104:105], v[172:173], v[144:145] op_sel_hi:[0,1,1]
	v_pk_fma_f32 v[110:111], v[104:105], v[236:237], v[110:111] op_sel_hi:[0,1,1]
	v_pk_fma_f32 v[104:105], v[104:105], v[116:117], v[106:107] op_sel_hi:[0,1,1]
	v_pk_fma_f32 v[2:3], v[2:3], v[108:109], v[66:67]
	v_pk_fma_f32 v[0:1], v[0:1], v[112:113], v[64:65]
	v_pk_fma_f32 v[6:7], v[6:7], v[118:119], v[62:63]
	v_pk_fma_f32 v[4:5], v[4:5], v[114:115], v[60:61]
	v_pk_fma_f32 v[8:9], v[8:9], v[122:123], v[56:57]
	v_pk_fma_f32 v[10:11], v[10:11], v[120:121], v[58:59]
	v_pk_fma_f32 v[26:27], v[26:27], v[138:139], v[42:43]
	v_pk_fma_f32 v[34:35], v[34:35], v[104:105], v[38:39]
	v_mov_b32_e32 v38, v1
	v_mov_b32_e32 v39, v5
	v_mov_b32_e32 v42, v3
	v_mov_b32_e32 v43, v7
	v_pk_fma_f32 v[20:21], v[20:21], v[134:135], v[44:45]
	v_pk_fma_f32 v[22:23], v[22:23], v[132:133], v[46:47]
	v_pk_fma_f32 v[24:25], v[24:25], v[136:137], v[40:41]
	v_pk_fma_f32 v[32:33], v[32:33], v[110:111], v[36:37]
	v_mov_b32_e32 v36, v0
	v_mov_b32_e32 v37, v4
	v_mov_b32_e32 v40, v2
	v_mov_b32_e32 v41, v6
	v_pk_mul_f32 v[44:45], v[10:11], v[10:11]
	v_pk_mul_f32 v[46:47], v[8:9], v[8:9]
	v_pk_mul_f32 v[38:39], v[38:39], v[38:39]
	v_pk_mul_f32 v[42:43], v[42:43], v[42:43]
	v_pk_fma_f32 v[14:15], v[14:15], v[126:127], v[50:51]
	v_pk_fma_f32 v[12:13], v[12:13], v[124:125], v[48:49]
	v_pk_mov_b32 v[60:61], v[46:47], v[44:45] op_sel:[1,0]
	v_mov_b32_e32 v47, v45
	v_pk_fma_f32 v[36:37], v[36:37], v[36:37], v[38:39]
	v_pk_fma_f32 v[38:39], v[40:41], v[40:41], v[42:43]
	v_pk_fma_f32 v[18:19], v[18:19], v[130:131], v[54:55]
	v_pk_fma_f32 v[16:17], v[16:17], v[128:129], v[52:53]
	v_mul_f32_e32 v48, v13, v13
	v_mul_f32_e32 v50, v15, v15
	v_pk_add_f32 v[40:41], v[60:61], v[46:47]
	v_pk_add_f32 v[36:37], v[36:37], v[38:39]
	v_mul_f32_e32 v59, v16, v16
	v_mul_f32_e32 v62, v17, v17
	v_mul_f32_e32 v63, v18, v18
	v_mul_f32_e32 v64, v19, v19
	v_pk_fma_f32 v[44:45], v[12:13], v[12:13], v[48:49] op_sel_hi:[1,1,0]
	v_pk_fma_f32 v[48:49], v[14:15], v[14:15], v[50:51] op_sel_hi:[1,1,0]
	v_pk_add_f32 v[38:39], v[40:41], v[40:41] op_sel:[0,1] op_sel_hi:[1,0]
	v_pk_add_f32 v[36:37], v[36:37], v[36:37] op_sel:[0,1] op_sel_hi:[1,0]
	v_pk_mul_f32 v[52:53], v[22:23], v[22:23]
	v_pk_mul_f32 v[54:55], v[20:21], v[20:21]
	v_mov_b32_e32 v45, v63
	v_mov_b32_e32 v49, v64
	v_mov_b32_e32 v39, v62
	v_mov_b32_e32 v37, v59
; #define GAS __attribute__((address_space(1)))
; __device__ __forceinline__ float dot4(f32x4 a, f32x4 b) { return (a.x * b.x + a.y * b.y) + (a.z * b.z + a.w * b.w); }
; __device__ __forceinline__ void phase12(KP kp, LAS unsigned char* lds, int wave, int bid, int G) {
;     ...
;             v[j] = xr[64 * j] + g2 * mo; s += dot4(v[j], v[j]); }
;         const float rstd = 1.0f / sqrtf(wave_sum(s) * (1.0f / DM) + EPS);
;         GAS f32x4* o = (GAS f32x4*)(KOUT() + (size_t)m * DM) + lane;
; #pragma unroll
;         for (int j = 0; j < 8; ++j) o[64 * j] = v[j] * rstd * *(const GAS f32x4*)(fg + 256 * j + 4 * lane);
	v_pk_mov_b32 v[50:51], v[54:55], v[52:53] op_sel:[1,0]
	v_mov_b32_e32 v55, v53
	v_pk_add_f32 v[40:41], v[44:45], v[48:49]
	v_pk_add_f32 v[36:37], v[36:37], v[38:39]
	v_mul_f32_e32 v56, v25, v25
	v_mul_f32_e32 v58, v27, v27
	v_pk_add_f32 v[42:43], v[50:51], v[54:55]
	v_pk_add_f32 v[36:37], v[36:37], v[40:41]
	v_mul_f32_e32 v65, v32, v32
	v_mul_f32_e32 v66, v33, v33
	v_mul_f32_e32 v67, v34, v34
	v_mul_f32_e32 v103, v35, v35
	v_pk_fma_f32 v[52:53], v[24:25], v[24:25], v[56:57] op_sel_hi:[1,1,0]
	v_pk_fma_f32 v[56:57], v[26:27], v[26:27], v[58:59] op_sel_hi:[1,1,0]
	v_pk_add_f32 v[42:43], v[42:43], v[42:43] op_sel:[0,1] op_sel_hi:[1,0]
	v_pk_add_f32 v[36:37], v[36:37], v[36:37] op_sel:[0,1] op_sel_hi:[1,0]
	v_mov_b32_e32 v53, v67
	v_mov_b32_e32 v57, v103
	v_mov_b32_e32 v43, v66
	v_mov_b32_e32 v37, v65
	v_pk_add_f32 v[44:45], v[52:53], v[56:57]
	v_pk_add_f32 v[36:37], v[36:37], v[42:43]
	s_nop 0
	v_pk_add_f32 v[36:37], v[36:37], v[44:45]
	s_nop 0
	v_add_f32_e32 v36, v36, v37
	s_nop 1
	v_add_f32_dpp v36, v36, v36 quad_perm:[1,0,3,2] row_mask:0xf bank_mask:0xf
	s_nop 1
	v_add_f32_dpp v36, v36, v36 quad_perm:[2,3,0,1] row_mask:0xf bank_mask:0xf
	s_nop 1
	v_add_f32_dpp v36, v36, v36 row_half_mirror row_mask:0xf bank_mask:0xf
	s_nop 1
	v_add_f32_dpp v36, v36, v36 row_mirror row_mask:0xf bank_mask:0xf
	v_mov_b32_e32 v37, v36
	s_nop 1
	v_permlane16_swap_b32_e32 v36, v37
	v_add_f32_e32 v36, v36, v37
	v_mov_b32_e32 v37, v36
	s_nop 1
	v_permlane32_swap_b32_e32 v36, v37
	v_add_f32_e32 v36, v36, v37
	global_load_dwordx4 v[44:47], v[72:73], off offset:1024
	global_load_dwordx4 v[48:51], v[72:73], off offset:2048
	global_load_dwordx4 v[52:55], v[72:73], off offset:3072
	global_load_dwordx4 v[56:59], v[82:83], off
	global_load_dwordx4 v[60:63], v[84:85], off
	global_load_dwordx4 v[64:67], v[86:87], off
	global_load_dwordx4 v[94:97], v[88:89], off
	v_fmamk_f32 v36, v36, 0x3a000000, v101
	v_mul_f32_e32 v37, 0x4f800000, v36
	v_cmp_gt_f32_e32 vcc, s22, v36
	s_nop 1
	v_cndmask_b32_e32 v36, v36, v37, vcc
	v_sqrt_f32_e32 v37, v36
	s_nop 0
	v_add_u32_e32 v38, -1, v37
	v_add_u32_e32 v39, 1, v37
	v_fma_f32 v40, -v38, v37, v36
	v_fma_f32 v41, -v39, v37, v36
	v_cmp_ge_f32_e64 s[0:1], 0, v40
	s_nop 1
	v_cndmask_b32_e64 v37, v37, v38, s[0:1]
	v_cmp_lt_f32_e64 s[0:1], 0, v41
	s_nop 1
	v_cndmask_b32_e64 v37, v37, v39, s[0:1]
	v_mul_f32_e32 v38, 0x37800000, v37
	v_cndmask_b32_e32 v37, v37, v38, vcc
	v_cmp_class_f32_e32 vcc, v36, v102
	s_nop 1
	v_cndmask_b32_e32 v36, v37, v36, vcc
	v_div_scale_f32 v37, s[0:1], v36, v36, 1.0
	v_rcp_f32_e32 v39, v37
	v_div_scale_f32 v38, vcc, 1.0, v36, 1.0
	v_fma_f32 v40, -v37, v39, 1.0
	v_fmac_f32_e32 v39, v40, v39
	v_mul_f32_e32 v40, v38, v39
	v_fma_f32 v41, -v37, v40, v38
	v_fmac_f32_e32 v40, v41, v39
	v_fma_f32 v37, -v37, v40, v38
	v_div_fmas_f32 v37, v37, v39, v40
	v_div_fixup_f32 v36, v37, v36, 1.0
	v_add_co_u32_e32 v38, vcc, s23, v92
	s_nop 1
	v_addc_co_u32_e32 v39, vcc, 0, v93, vcc
	s_waitcnt vmcnt(0)
	v_pk_mul_f32 v[0:1], v[0:1], v[36:37] op_sel_hi:[1,0]
	v_pk_mul_f32 v[2:3], v[2:3], v[36:37] op_sel_hi:[1,0]
	v_pk_mul_f32 v[0:1], v[28:29], v[0:1]
	v_pk_mul_f32 v[2:3], v[30:31], v[2:3]
	global_store_dwordx4 v[92:93], v[0:3], off
	v_pk_mul_f32 v[4:5], v[4:5], v[36:37] op_sel_hi:[1,0]
	v_pk_mul_f32 v[6:7], v[6:7], v[36:37] op_sel_hi:[1,0]
	v_pk_mul_f32 v[4:5], v[44:45], v[4:5]
	v_pk_mul_f32 v[6:7], v[46:47], v[6:7]
	global_store_dwordx4 v[92:93], v[4:7], off offset:1024
	v_pk_mul_f32 v[8:9], v[8:9], v[36:37] op_sel_hi:[1,0]
	v_pk_mul_f32 v[10:11], v[10:11], v[36:37] op_sel_hi:[1,0]
	v_pk_mul_f32 v[8:9], v[48:49], v[8:9]
	v_pk_mul_f32 v[10:11], v[50:51], v[10:11]
	global_store_dwordx4 v[92:93], v[8:11], off offset:2048
	v_pk_mul_f32 v[12:13], v[12:13], v[36:37] op_sel_hi:[1,0]
	v_pk_mul_f32 v[14:15], v[14:15], v[36:37] op_sel_hi:[1,0]
	v_pk_mul_f32 v[12:13], v[52:53], v[12:13]
	v_pk_mul_f32 v[14:15], v[54:55], v[14:15]
	global_store_dwordx4 v[92:93], v[12:15], off offset:3072
	v_pk_mul_f32 v[16:17], v[16:17], v[36:37] op_sel_hi:[1,0]
	v_pk_mul_f32 v[18:19], v[18:19], v[36:37] op_sel_hi:[1,0]
	v_pk_mul_f32 v[16:17], v[56:57], v[16:17]
	v_pk_mul_f32 v[18:19], v[58:59], v[18:19]
	global_store_dwordx4 v[38:39], v[16:19], off
	v_pk_mul_f32 v[20:21], v[20:21], v[36:37] op_sel_hi:[1,0]
	v_pk_mul_f32 v[22:23], v[22:23], v[36:37] op_sel_hi:[1,0]
	v_pk_mul_f32 v[20:21], v[60:61], v[20:21]
	v_pk_mul_f32 v[22:23], v[62:63], v[22:23]
	global_store_dwordx4 v[38:39], v[20:23], off offset:1024
	v_pk_mul_f32 v[24:25], v[24:25], v[36:37] op_sel_hi:[1,0]
	v_pk_mul_f32 v[26:27], v[26:27], v[36:37] op_sel_hi:[1,0]
	v_pk_mul_f32 v[24:25], v[64:65], v[24:25]
	v_pk_mul_f32 v[26:27], v[66:67], v[26:27]
	global_store_dwordx4 v[38:39], v[24:27], off offset:2048
	v_pk_mul_f32 v[32:33], v[32:33], v[36:37] op_sel_hi:[1,0]
	v_pk_mul_f32 v[34:35], v[34:35], v[36:37] op_sel_hi:[1,0]
	v_pk_mul_f32 v[32:33], v[94:95], v[32:33]
	v_pk_mul_f32 v[34:35], v[96:97], v[34:35]
	global_store_dwordx4 v[38:39], v[32:35], off offset:3072
	s_cbranch_scc1 .LBB0_4682
